# baseline (speedup 1.0000x reference)
.LBB4_43:
	s_or_b64 exec, exec, s[0:1]
	ds_read_b128 v[26:29], v86
	ds_read_b128 v[22:25], v86 offset:1024
	s_setprio 1
	s_waitcnt lgkmcnt(0)
	v_mfma_f32_16x16x32_f16 v[30:33], v[26:29], v[40:43], 0
	v_mfma_f32_16x16x32_f16 v[34:37], v[26:29], v[48:51], 0
	v_mfma_f32_16x16x32_f16 v[106:109], v[26:29], v[56:59], 0
	v_mfma_f32_16x16x32_f16 v[30:33], v[22:25], v[44:47], v[30:33]
	v_mfma_f32_16x16x32_f16 v[34:37], v[22:25], v[52:55], v[34:37]
	v_mfma_f32_16x16x32_f16 v[106:109], v[22:25], v[60:63], v[106:109]
	s_add_u32 s2, s20, 0x16900
	s_addc_u32 s3, s21, 0
	s_nop 3
	v_cvt_pk_f16_f32 v30, v30, v31
	v_cvt_pk_f16_f32 v31, v32, v33
	ds_write_b64 v88, v[30:31]
	v_cvt_pk_f16_f32 v34, v34, v35
	v_cvt_pk_f16_f32 v35, v36, v37
	ds_write_b64 v90, v[34:35]
	s_nop 0
	v_cvt_pk_f16_f32 v106, v106, v107
	v_cvt_pk_f16_f32 v107, v108, v109
	ds_write_b64 v92, v[106:107]
	v_mbcnt_lo_u32_b32 v126, -1, 0
	v_mbcnt_hi_u32_b32 v126, -1, v126
	v_bfe_u32 v126, v126, 4, 2
	v_lshl_or_b32 v126, v126, 2, s101
	v_or_b32_e32 v40, 0, v126
	v_lshlrev_b32_e32 v40, 16, v40
	v_mov_b32_e32 v41, 0
	v_or_b32_e32 v42, 1, v126
	v_lshlrev_b32_e32 v42, 16, v42
	v_mov_b32_e32 v43, 0
	v_or_b32_e32 v44, 2, v126
	v_lshlrev_b32_e32 v44, 16, v44
	v_mov_b32_e32 v45, 0
	v_or_b32_e32 v46, 3, v126
	v_lshlrev_b32_e32 v46, 16, v46
	v_mov_b32_e32 v47, 0
	v_or_b32_e32 v48, 16, v126
	v_lshlrev_b32_e32 v48, 16, v48
	v_mov_b32_e32 v49, 0
	v_or_b32_e32 v50, 17, v126
	v_lshlrev_b32_e32 v50, 16, v50
	v_mov_b32_e32 v51, 0
	v_or_b32_e32 v52, 18, v126
	v_lshlrev_b32_e32 v52, 16, v52
	v_mov_b32_e32 v53, 0
	v_or_b32_e32 v54, 19, v126
	v_lshlrev_b32_e32 v54, 16, v54
	v_mov_b32_e32 v55, 0
	v_or_b32_e32 v56, 32, v126
	v_lshlrev_b32_e32 v56, 16, v56
	v_mov_b32_e32 v57, 0
	v_or_b32_e32 v58, 33, v126
	v_lshlrev_b32_e32 v58, 16, v58
	v_mov_b32_e32 v59, 0
	v_or_b32_e32 v60, 34, v126
	v_lshlrev_b32_e32 v60, 16, v60
	v_mov_b32_e32 v61, 0
	v_or_b32_e32 v62, 35, v126
	v_lshlrev_b32_e32 v62, 16, v62
	v_mov_b32_e32 v63, 0
	s_branch .Lnarrow_cont

.Lnarrow_cont:
	s_setprio 0
	v_readfirstlane_b32 s0, v99
	s_ashr_i32 s10, s0, 1
	s_mul_i32 s12, s10, 18
	s_and_b32 s11, s0, 1
	s_add_i32 s0, s12, 0x2d0
	s_ashr_i32 s1, s0, 31
	s_lshl_b64 s[0:1], s[0:1], 3
	s_add_u32 s8, s2, s0
	s_addc_u32 s9, s3, s1
	s_add_i32 s0, s12, 0x318
	s_ashr_i32 s1, s0, 31
	s_lshl_b64 s[0:1], s[0:1], 3
	s_add_u32 s0, s2, s0
	s_addc_u32 s1, s3, s1
	s_lshl_b32 s2, s10, 4
	s_lshl_b32 s11, s11, 3
	s_or_b32 s10, s11, s2
	s_waitcnt lgkmcnt(0)
	s_barrier
	v_add_u32_e32 v0, s10, v80
	ds_read2_b64 v[22:25], v0 offset1:8
	s_load_dwordx2 s[2:3], s[8:9], s11 offset:0x0
	s_load_dwordx2 s[12:13], s[8:9], s11 offset:0x10
	s_load_dwordx2 s[14:15], s[8:9], s11 offset:0x20
	s_load_dwordx2 s[16:17], s[8:9], s11 offset:0x30
	v_add_u32_e32 v34, 0x800, v0
	v_mov_b32_e32 v77, 1.0
	s_waitcnt lgkmcnt(0)
	v_pk_fma_f16 v23, v23, s3, 0
	v_pk_fma_f16 v22, v22, s2, 0
	s_load_dwordx2 s[2:3], s[0:1], s11 offset:0x0
	s_load_dwordx2 s[18:19], s[0:1], s11 offset:0x30
	ds_read2_b64 v[26:29], v0 offset0:18 offset1:26
	s_load_dwordx2 s[20:21], s[0:1], s11 offset:0x10
	s_load_dwordx2 s[22:23], s[0:1], s11 offset:0x20
	s_load_dwordx2 s[24:25], s[8:9], s11 offset:0x80
	s_waitcnt lgkmcnt(0)
	v_pk_fma_f16 v30, v24, s2, 0
	v_pk_fma_f16 v31, v25, s3, 0
	v_pk_fma_f16 v32, v26, s12, v22
	v_pk_fma_f16 v33, v27, s13, v23
	ds_read2_b64 v[22:25], v0 offset0:36 offset1:44
	v_pk_fma_f16 v31, v29, s21, v31
	v_pk_fma_f16 v30, v28, s20, v30
	ds_read2_b64 v[26:29], v34 offset0:68 offset1:76
	v_add_u32_e32 v0, 0x1000, v0
	s_waitcnt lgkmcnt(1)
	v_pk_fma_f16 v23, v23, s15, v33
	v_pk_fma_f16 v22, v22, s14, v32
	v_pk_fma_f16 v24, v24, s22, v30
	v_pk_fma_f16 v25, v25, s23, v31
	s_waitcnt lgkmcnt(0)
	v_pk_fma_f16 v30, v26, s16, v22
	v_pk_fma_f16 v31, v27, s17, v23
	s_load_dwordx2 s[12:13], s[0:1], s11 offset:0x40
	s_load_dwordx2 s[14:15], s[0:1], s11 offset:0x50
	s_load_dwordx2 s[2:3], s[0:1], s11 offset:0x60
	v_pk_fma_f16 v32, v29, s19, v25
	v_pk_fma_f16 v33, v28, s18, v24
	ds_read2_b64 v[22:25], v34 offset0:86 offset1:94
	s_load_dwordx2 s[16:17], s[8:9], s11 offset:0x40
	ds_read2_b64 v[26:29], v34 offset0:104 offset1:112
	s_load_dwordx2 s[18:19], s[8:9], s11 offset:0x50
	s_load_dwordx2 s[20:21], s[8:9], s11 offset:0x60
	s_nop 0
	s_load_dwordx2 s[8:9], s[8:9], s11 offset:0x70
	s_waitcnt lgkmcnt(0)
	v_pk_fma_f16 v34, v24, s12, v33
	v_pk_fma_f16 v23, v23, s17, v31
	v_pk_fma_f16 v22, v22, s16, v30
	v_pk_fma_f16 v30, v25, s13, v32
	v_pk_fma_f16 v35, v26, s18, v22
	v_pk_fma_f16 v36, v27, s19, v23
	ds_read2_b64 v[22:25], v0 offset0:136 offset1:144
	v_pk_fma_f16 v38, v29, s15, v30
	ds_read2_b64 v[30:33], v0 offset0:154 offset1:162
	v_pk_fma_f16 v76, v28, s14, v34
	ds_read2_b64 v[26:29], v0 offset0:172 offset1:180
	s_waitcnt lgkmcnt(2)
	v_pk_fma_f16 v0, v23, s21, v36
	v_pk_fma_f16 v22, v22, s20, v35
	s_waitcnt lgkmcnt(1)
	v_pk_fma_f16 v0, v31, s9, v0
	v_pk_fma_f16 v22, v30, s8, v22
	s_waitcnt lgkmcnt(0)
	v_pk_fma_f16 v0, v27, s25, v0
	v_pk_fma_f16 v27, v26, s24, v22
	s_load_dwordx2 s[8:9], s[0:1], s11 offset:0x70
	s_nop 0
	s_load_dwordx2 s[0:1], s[0:1], s11 offset:0x80
	s_mov_b32 s11, 0x3e6d3387
	v_cvt_f32_f16_e32 v31, v27
	v_cvt_f32_f16_sdwa v35, v27 dst_sel:DWORD dst_unused:UNUSED_PAD src0_sel:WORD_1
	v_fma_mix_f32 v26, |v27|, s11, v77 op_sel_hi:[1,0,0]
	v_fma_mix_f32 v27, |v27|, s11, v77 op_sel:[1,0,0] op_sel_hi:[1,0,0]
	v_rcp_f32_e32 v26, v26
	v_rcp_f32_e32 v27, v27
	s_mov_b32 s12, 0xbf3a00e3
	v_and_b32_e32 v22, 0x7fffffff, v31
	v_mul_f32_e32 v30, 0x3f596d27, v31
	v_max_f32_e32 v34, 0, v31
	s_mov_b32 s14, 0x3f07dc22
	v_mov_b64_e32 v[36:37], s[12:13]
	v_mul_f32_e32 v31, 0x3f596d27, v35
	v_mul_f32_e64 v30, v30, -v30
	v_pk_fma_f32 v[72:73], v[26:27], s[14:15], v[36:37] op_sel_hi:[1,0,0]
	s_mov_b32 s12, 0x3f35f0e3
	v_mul_f32_e64 v31, v31, -v31
	v_exp_f32_e32 v30, v30
	v_pk_fma_f32 v[72:73], v[72:73], v[26:27], s[12:13] op_sel_hi:[1,1,0]
	s_mov_b32 s16, 0xbe11a98e
	v_exp_f32_e32 v31, v31
	v_pk_fma_f32 v[72:73], v[72:73], v[26:27], s[16:17] op_sel_hi:[1,1,0]
	s_mov_b32 s18, 0x3e027906
	v_pk_fma_f32 v[72:73], v[72:73], v[26:27], s[18:19] op_sel_hi:[1,1,0]
	v_and_b32_e32 v23, 0x7fffffff, v35
	v_pk_mul_f32 v[26:27], v[26:27], v[72:73]
	v_max_f32_e32 v35, 0, v35
	v_pk_mul_f32 v[26:27], v[30:31], v[26:27]
	v_cvt_f32_f16_e32 v31, v0
	v_cvt_f32_f16_sdwa v72, v0 dst_sel:DWORD dst_unused:UNUSED_PAD src0_sel:WORD_1
	v_pk_fma_f32 v[22:23], v[22:23], v[26:27], v[34:35] neg_lo:[1,0,0] neg_hi:[1,0,0]
	v_fma_mix_f32 v26, |v0|, s11, v77 op_sel_hi:[1,0,0]
	v_fma_mix_f32 v0, |v0|, s11, v77 op_sel:[1,0,0] op_sel_hi:[1,0,0]
	v_rcp_f32_e32 v26, v26
	v_rcp_f32_e32 v27, v0
	v_mul_f32_e32 v30, 0x3f596d27, v31
	v_mul_f32_e64 v0, v30, -v30
	v_exp_f32_e32 v30, v0
	v_mul_f32_e32 v0, 0x3f596d27, v72
	v_pk_fma_f32 v[36:37], v[26:27], s[14:15], v[36:37] op_sel_hi:[1,0,0]
	v_mul_f32_e64 v0, v0, -v0
	v_cvt_pk_f16_f32 v73, v22, v23
	v_and_b32_e32 v22, 0x7fffffff, v31
	v_max_f32_e32 v34, 0, v31
	v_pk_fma_f32 v[36:37], v[36:37], v[26:27], s[12:13] op_sel_hi:[1,1,0]
	v_exp_f32_e32 v31, v0
	v_pk_fma_f32 v[36:37], v[36:37], v[26:27], s[16:17] op_sel_hi:[1,1,0]
	v_and_b32_e32 v23, 0x7fffffff, v72
	v_pk_fma_f32 v[36:37], v[36:37], v[26:27], s[18:19] op_sel_hi:[1,1,0]
	v_max_f32_e32 v35, 0, v72
	v_pk_mul_f32 v[26:27], v[26:27], v[36:37]
	s_nop 0
	v_pk_mul_f32 v[26:27], v[30:31], v[26:27]
	s_nop 0
	v_pk_fma_f32 v[22:23], v[22:23], v[26:27], v[34:35] neg_lo:[1,0,0] neg_hi:[1,0,0]
	s_nop 0
	v_cvt_pk_f16_f32 v0, v22, v23
	v_pk_fma_f16 v22, v24, s2, v76
	v_pk_fma_f16 v23, v25, s3, v38
	s_waitcnt lgkmcnt(0)
	v_pk_fma_f16 v22, v32, s8, v22
	v_pk_fma_f16 v23, v33, s9, v23
	v_pk_fma_f16 v22, v28, s0, v22
	v_pk_fma_f16 v23, v29, s1, v23
	v_pk_mul_f16 v22, v22, v73
	v_pk_mul_f16 v23, v23, v0
	v_add_u32_e32 v0, s10, v78
	ds_write_b64 v0, v[22:23]
	s_and_saveexec_b64 s[0:1], s[4:5]
	s_cbranch_execz .LBB4_118
	s_waitcnt vmcnt(0)
	ds_write_b128 v39, v[18:21] offset:8192
